# compression: first 16 W1 fragment loads issued at the top of the unit loop (hidden behind slab staging); on top of rt14
# baseline (speedup 1.0000x reference)
; #define GAS __attribute__((address_space(1)))
; #define LAS __attribute__((address_space(3)))
; __device__ __forceinline__ void compress_mfma_phase(Frame& F, int l, bf16* CMP) {
;     ...
;     for (int unit = F.bx; unit < 2 * BATCH * NG * 8; unit += F.G) {
;         const int nb = unit & 7, g = (unit >> 3) & 3, b = (unit >> 5) & 3, kv = unit >> 7;
;         const bf16* W1T = (const bf16*)(F.ws + WS_W + (size_t)l * LW_BYTES + LW_PHI1) + (size_t)kv * 128 * 2048;
;         const bf16* W2T = (const bf16*)(F.ws + WS_W + (size_t)l * LW_BYTES + LW_PHI2) + (size_t)kv * 64 * 128;
;         const float* b1e = (const float*)(F.ws + WS_SMALL) + ((size_t)l * 2 + kv) * 16 * 128;
;         const int tok0 = 512 * nb, zc = (kv ? Z_VC : Z_KC) + g * 64;
;         { u32x4 sv[9];
; #pragma unroll
;           for (int q = 0; q < 9; ++q) { const int i = F.tid + q * NTHR; const int ti = i >> 3, ch = i & 7, tk = tok0 + ti; const bool ok = i < 528 * 8 && tk < SEQ;
;               sv[q] = *(const GAS u32x4*)(Z + (size_t)(b * SEQ + (ok ? tk : 0)) * NZ + zc + 8 * ch); if (!ok) sv[q] = (u32x4){0u, 0u, 0u, 0u}; }
; #pragma unroll
;           for (int q = 0; q < 9; ++q) { const int i = F.tid + q * NTHR; const int ti = i >> 3, ch = i & 7;
;               if (i < 528 * 8) *(LAS u32x4*)(XS + ((ti & 15) * 33 + (ti >> 4)) * XP + ch * 16) = sv[q]; } }
;     ...
;         const bf16* wrow = W1T + (size_t)(32 * ct + r32) * 2048 + 8 * h;
.LBB0_369:
	s_ashr_i32 s100, s73, 7
	s_ashr_i32 s101, s100, 31
	s_lshl_b64 s[100:101], s[100:101], 19
	v_lshl_add_u64 v[220:221], v[38:39], 0, s[100:101]
	global_load_dwordx4 v[138:141], v[220:221], off
	global_load_dwordx4 v[142:145], v[220:221], off offset:32
	global_load_dwordx4 v[146:149], v[220:221], off offset:64
	global_load_dwordx4 v[150:153], v[220:221], off offset:96
	global_load_dwordx4 v[154:157], v[220:221], off offset:128
	global_load_dwordx4 v[158:161], v[220:221], off offset:160
	global_load_dwordx4 v[162:165], v[220:221], off offset:192
	global_load_dwordx4 v[166:169], v[220:221], off offset:224
	global_load_dwordx4 v[170:173], v[220:221], off offset:256
	global_load_dwordx4 v[174:177], v[220:221], off offset:288
	global_load_dwordx4 v[178:181], v[220:221], off offset:320
	global_load_dwordx4 v[182:185], v[220:221], off offset:352
	global_load_dwordx4 v[186:189], v[220:221], off offset:384
	global_load_dwordx4 v[190:193], v[220:221], off offset:416
	global_load_dwordx4 v[200:203], v[220:221], off offset:448
	global_load_dwordx4 v[204:207], v[220:221], off offset:480
	s_and_b32 s92, s73, 7
	s_lshl_b32 s9, s92, 9
	s_bfe_u32 s8, s73, 0x20003
	s_bfe_u32 s16, s73, 0x20005
	v_add_u32_e32 v0, s9, v57
	s_movk_i32 s3, 0x1000
	s_cmpk_lt_u32 s73, 0x80
	s_movk_i32 s0, 0x3200
	v_cmp_gt_i32_e32 vcc, s3, v0
	s_cselect_b32 s0, 0x3000, s0
	s_lshl_b32 s1, s8, 7
	s_and_b64 s[68:69], s[40:41], vcc
	s_lshl_b32 s93, s16, 12
	s_or_b32 s88, s1, s0
	v_cndmask_b32_e64 v0, 0, v0, s[68:69]
	v_lshl_add_u64 v[44:45], v[36:37], 0, s[88:89]
	v_add_u32_e32 v0, s93, v0
	v_mad_i64_i32 v[2:3], s[0:1], v0, s33, v[44:45]
	v_add_u32_e32 v0, s9, v58
	v_cmp_gt_i32_e32 vcc, s3, v0
	s_and_b64 s[66:67], s[42:43], vcc
	v_cndmask_b32_e64 v0, 0, v0, s[66:67]
	v_add_u32_e32 v0, s93, v0
	v_mad_i64_i32 v[4:5], s[0:1], v0, s33, v[44:45]
	v_add_u32_e32 v0, s9, v59
	v_cmp_gt_i32_e32 vcc, s3, v0
	s_and_b64 s[64:65], s[44:45], vcc
	v_cndmask_b32_e64 v0, 0, v0, s[64:65]
	v_add_u32_e32 v0, s93, v0
	global_load_dwordx4 v[30:33], v[2:3], off
	global_load_dwordx4 v[26:29], v[4:5], off
	v_mad_i64_i32 v[2:3], s[0:1], v0, s33, v[44:45]
	v_add_u32_e32 v0, s9, v60
	v_cmp_gt_i32_e32 vcc, s3, v0
	s_and_b64 s[62:63], s[46:47], vcc
	v_cndmask_b32_e64 v0, 0, v0, s[62:63]
	v_add_u32_e32 v0, s93, v0
	v_mad_i64_i32 v[4:5], s[0:1], v0, s33, v[44:45]
	v_add_u32_e32 v0, s9, v61
	v_cmp_gt_i32_e32 vcc, s3, v0
	s_and_b64 s[60:61], s[48:49], vcc
	v_cndmask_b32_e64 v0, 0, v0, s[60:61]
	v_add_u32_e32 v0, s93, v0
	global_load_dwordx4 v[22:25], v[2:3], off
	global_load_dwordx4 v[18:21], v[4:5], off
	v_mad_i64_i32 v[2:3], s[0:1], v0, s33, v[44:45]
	v_add_u32_e32 v0, s9, v62
	v_cmp_gt_i32_e32 vcc, s3, v0
	s_and_b64 s[58:59], s[50:51], vcc
	v_cndmask_b32_e64 v0, 0, v0, s[58:59]
	v_add_u32_e32 v0, s93, v0
	v_mad_i64_i32 v[4:5], s[0:1], v0, s33, v[44:45]
	v_add_u32_e32 v0, s9, v63
	v_cmp_gt_i32_e32 vcc, s3, v0
	s_and_b64 s[0:1], s[52:53], vcc
	v_cndmask_b32_e64 v0, 0, v0, s[0:1]
	v_add_u32_e32 v0, s93, v0
	global_load_dwordx4 v[14:17], v[2:3], off
	global_load_dwordx4 v[10:13], v[4:5], off
	v_mad_i64_i32 v[2:3], s[70:71], v0, s33, v[44:45]
	v_add_u32_e32 v0, s9, v64
	v_cmp_gt_i32_e32 vcc, s3, v0
	s_and_b64 vcc, s[38:39], vcc
	s_movk_i32 s2, 0x1000
	v_cndmask_b32_e32 v0, 0, v0, vcc
	v_add_u32_e32 v0, s93, v0
	v_mad_i64_i32 v[4:5], s[70:71], v0, s33, v[44:45]
	global_load_dwordx4 v[6:9], v[2:3], off
	s_nop 0
	global_load_dwordx4 v[2:5], v[4:5], off
	s_and_saveexec_b64 s[78:79], s[54:55]
	s_cbranch_execz .LBB0_385
	v_add_u32_e32 v0, s9, v65
	v_cmp_gt_i32_e64 s[70:71], s2, v0
	s_nop 1
	v_cndmask_b32_e64 v0, 0, v0, s[70:71]
	v_add_u32_e32 v0, s93, v0
	v_mad_i64_i32 v[44:45], s[2:3], v0, s33, v[44:45]
	global_load_dwordx4 v[80:83], v[44:45], off
	s_waitcnt vmcnt(0)
	v_cndmask_b32_e64 v83, 0, v83, s[70:71]
	v_cndmask_b32_e64 v82, 0, v82, s[70:71]
	v_cndmask_b32_e64 v81, 0, v81, s[70:71]
	v_cndmask_b32_e64 v80, 0, v80, s[70:71]
	ds_write_b128 v66, v[80:83]
	s_or_b64 exec, exec, s[78:79]
	s_and_saveexec_b64 s[70:71], s[40:41]
	s_cbranch_execnz .LBB0_386

; #define CMP_LOADW(dst, lb) { _Pragma("unroll") for (int q = 0; q < 4; ++q) _Pragma("unroll") for (int ks = 0; ks < 4; ++ks) dst[q][ks] = *(const GAS bf16x8*)(wrow + ((lb) + q) * 64 + 16 * ks); }
; #define CMP_MMA(src, lb) { _Pragma("unroll") for (int q = 0; q < 4; ++q) { const int ll = (lb) + q; const LAS unsigned char* xr = XS + ((ll & 15) * 33 + (ll >> 4) + r32) * XP + 16 * h; \
;             _Pragma("unroll") for (int ks = 0; ks < 4; ++ks) { const bf16x8 af = *(const LAS bf16x8*)(xr + 32 * ks); acc = __builtin_amdgcn_mfma_f32_32x32x16_bf16(af, src[q][ks], acc, 0, 0, 0); } } }
; __device__ __forceinline__ void compress_mfma_phase(Frame& F, int l, bf16* CMP) {
;     ...
;         __syncthreads();
;         const int ct = w & 3, lh = w >> 2;
;         f32x16 acc;
; #pragma unroll
;         for (int i = 0; i < 16; ++i) acc[i] = 0.f;
;         const bf16* wrow = W1T + (size_t)(32 * ct + r32) * 2048 + 8 * h;
;         { bf16x8 wa[4][4], wb[4][4]; const int l0 = 16 * lh;
;     ...
;           CMP_LOADW(wa, l0) CMP_LOADW(wb, l0 + 4) CMP_MMA(wa, l0) CMP_LOADW(wa, l0 + 8) CMP_MMA(wb, l0 + 4) CMP_LOADW(wb, l0 + 12) CMP_MMA(wa, l0 + 8) CMP_MMA(wb, l0 + 12)
.LBB0_379:
	s_or_b64 exec, exec, s[0:1]
	s_ashr_i32 s0, s73, 7
	s_ashr_i32 s1, s0, 31
	s_lshl_b64 s[2:3], s[0:1], 19
	s_waitcnt vmcnt(0)
	v_lshl_add_u64 v[18:19], v[38:39], 0, s[2:3]
	s_waitcnt lgkmcnt(0)
	s_barrier
	ds_read_b128 v[208:211], v48
	ds_read_b128 v[212:215], v48 offset:32
	ds_read_b128 v[216:219], v48 offset:64
	ds_read_b128 v[80:83], v48 offset:96
	ds_read_b128 v[84:87], v48 offset:4752
	ds_read_b128 v[88:91], v48 offset:4784
	ds_read_b128 v[92:95], v48 offset:4816
	ds_read_b128 v[96:99], v48 offset:4848
	s_waitcnt vmcnt(15) lgkmcnt(7)
	v_mfma_f32_32x32x16_bf16 v[2:17], v[208:211], v[138:141], 0
	global_load_dwordx4 v[138:141], v[220:221], off offset:512
	ds_read_b128 v[208:211], v48 offset:9504
	s_waitcnt vmcnt(15) lgkmcnt(7)
	v_mfma_f32_32x32x16_bf16 v[2:17], v[212:215], v[142:145], v[2:17]
	global_load_dwordx4 v[142:145], v[220:221], off offset:544
	ds_read_b128 v[212:215], v48 offset:9536
	s_waitcnt vmcnt(15) lgkmcnt(7)
	v_mfma_f32_32x32x16_bf16 v[2:17], v[216:219], v[146:149], v[2:17]
	global_load_dwordx4 v[146:149], v[220:221], off offset:576
	ds_read_b128 v[216:219], v48 offset:9568
	s_waitcnt vmcnt(15) lgkmcnt(7)
	v_mfma_f32_32x32x16_bf16 v[2:17], v[80:83], v[150:153], v[2:17]
	global_load_dwordx4 v[150:153], v[220:221], off offset:608
	ds_read_b128 v[80:83], v48 offset:9600
	s_waitcnt vmcnt(15) lgkmcnt(7)
	v_mfma_f32_32x32x16_bf16 v[2:17], v[84:87], v[154:157], v[2:17]
	global_load_dwordx4 v[154:157], v[220:221], off offset:640
	ds_read_b128 v[84:87], v48 offset:14256
	s_waitcnt vmcnt(15) lgkmcnt(7)
	v_mfma_f32_32x32x16_bf16 v[2:17], v[88:91], v[158:161], v[2:17]
	global_load_dwordx4 v[158:161], v[220:221], off offset:672
	ds_read_b128 v[88:91], v48 offset:14288
	s_waitcnt vmcnt(15) lgkmcnt(7)
	v_mfma_f32_32x32x16_bf16 v[2:17], v[92:95], v[162:165], v[2:17]
	global_load_dwordx4 v[162:165], v[220:221], off offset:704
	ds_read_b128 v[92:95], v48 offset:14320
	s_waitcnt vmcnt(15) lgkmcnt(7)
	v_mfma_f32_32x32x16_bf16 v[2:17], v[96:99], v[166:169], v[2:17]
	global_load_dwordx4 v[166:169], v[220:221], off offset:736
	ds_read_b128 v[96:99], v48 offset:14352
	s_waitcnt vmcnt(15) lgkmcnt(7)
	v_mfma_f32_32x32x16_bf16 v[2:17], v[208:211], v[170:173], v[2:17]
	global_load_dwordx4 v[170:173], v[220:221], off offset:768
	ds_read_b128 v[208:211], v48 offset:19008
	s_waitcnt vmcnt(15) lgkmcnt(7)
	v_mfma_f32_32x32x16_bf16 v[2:17], v[212:215], v[174:177], v[2:17]
	global_load_dwordx4 v[174:177], v[220:221], off offset:800
	ds_read_b128 v[212:215], v48 offset:19040
	s_waitcnt vmcnt(15) lgkmcnt(7)
	v_mfma_f32_32x32x16_bf16 v[2:17], v[216:219], v[178:181], v[2:17]
	global_load_dwordx4 v[178:181], v[220:221], off offset:832
	ds_read_b128 v[216:219], v48 offset:19072
	s_waitcnt vmcnt(15) lgkmcnt(7)
	v_mfma_f32_32x32x16_bf16 v[2:17], v[80:83], v[182:185], v[2:17]
	global_load_dwordx4 v[182:185], v[220:221], off offset:864
	ds_read_b128 v[80:83], v48 offset:19104
	s_waitcnt vmcnt(15) lgkmcnt(7)
	v_mfma_f32_32x32x16_bf16 v[2:17], v[84:87], v[186:189], v[2:17]
	global_load_dwordx4 v[186:189], v[220:221], off offset:896
	ds_read_b128 v[84:87], v48 offset:23760
	s_waitcnt vmcnt(15) lgkmcnt(7)
	v_mfma_f32_32x32x16_bf16 v[2:17], v[88:91], v[190:193], v[2:17]
	global_load_dwordx4 v[190:193], v[220:221], off offset:928
	ds_read_b128 v[88:91], v48 offset:23792
	s_waitcnt vmcnt(15) lgkmcnt(7)
	v_mfma_f32_32x32x16_bf16 v[2:17], v[92:95], v[200:203], v[2:17]
	global_load_dwordx4 v[200:203], v[220:221], off offset:960
	ds_read_b128 v[92:95], v48 offset:23824
	s_waitcnt vmcnt(15) lgkmcnt(7)
	v_mfma_f32_32x32x16_bf16 v[2:17], v[96:99], v[204:207], v[2:17]
	global_load_dwordx4 v[204:207], v[220:221], off offset:992
	ds_read_b128 v[96:99], v48 offset:23856
	s_waitcnt vmcnt(15) lgkmcnt(7)
	v_mfma_f32_32x32x16_bf16 v[2:17], v[208:211], v[138:141], v[2:17]
	global_load_dwordx4 v[138:141], v[220:221], off offset:1024
	ds_read_b128 v[208:211], v48 offset:28512
	s_waitcnt vmcnt(15) lgkmcnt(7)
	v_mfma_f32_32x32x16_bf16 v[2:17], v[212:215], v[142:145], v[2:17]
	global_load_dwordx4 v[142:145], v[220:221], off offset:1056
	ds_read_b128 v[212:215], v48 offset:28544
	s_waitcnt vmcnt(15) lgkmcnt(7)
	v_mfma_f32_32x32x16_bf16 v[2:17], v[216:219], v[146:149], v[2:17]
	global_load_dwordx4 v[146:149], v[220:221], off offset:1088
	ds_read_b128 v[216:219], v48 offset:28576
	s_waitcnt vmcnt(15) lgkmcnt(7)
	v_mfma_f32_32x32x16_bf16 v[2:17], v[80:83], v[150:153], v[2:17]
	global_load_dwordx4 v[150:153], v[220:221], off offset:1120
	ds_read_b128 v[80:83], v48 offset:28608
	s_waitcnt vmcnt(15) lgkmcnt(7)
	v_mfma_f32_32x32x16_bf16 v[2:17], v[84:87], v[154:157], v[2:17]
	global_load_dwordx4 v[154:157], v[220:221], off offset:1152
	ds_read_b128 v[84:87], v48 offset:33264
	s_waitcnt vmcnt(15) lgkmcnt(7)
	v_mfma_f32_32x32x16_bf16 v[2:17], v[88:91], v[158:161], v[2:17]
	global_load_dwordx4 v[158:161], v[220:221], off offset:1184
	ds_read_b128 v[88:91], v48 offset:33296
	s_waitcnt vmcnt(15) lgkmcnt(7)
	v_mfma_f32_32x32x16_bf16 v[2:17], v[92:95], v[162:165], v[2:17]
	global_load_dwordx4 v[162:165], v[220:221], off offset:1216
	ds_read_b128 v[92:95], v48 offset:33328
	s_waitcnt vmcnt(15) lgkmcnt(7)
	v_mfma_f32_32x32x16_bf16 v[2:17], v[96:99], v[166:169], v[2:17]
	global_load_dwordx4 v[166:169], v[220:221], off offset:1248
	ds_read_b128 v[96:99], v48 offset:33360
	s_waitcnt vmcnt(15) lgkmcnt(7)
	v_mfma_f32_32x32x16_bf16 v[2:17], v[208:211], v[170:173], v[2:17]
	global_load_dwordx4 v[170:173], v[220:221], off offset:1280
	ds_read_b128 v[208:211], v48 offset:38016
	s_waitcnt vmcnt(15) lgkmcnt(7)
; #define CMP_LOADW(dst, lb) { _Pragma("unroll") for (int q = 0; q < 4; ++q) _Pragma("unroll") for (int ks = 0; ks < 4; ++ks) dst[q][ks] = *(const GAS bf16x8*)(wrow + ((lb) + q) * 64 + 16 * ks); }
; #define CMP_MMA(src, lb) { _Pragma("unroll") for (int q = 0; q < 4; ++q) { const int ll = (lb) + q; const LAS unsigned char* xr = XS + ((ll & 15) * 33 + (ll >> 4) + r32) * XP + 16 * h; \
;             _Pragma("unroll") for (int ks = 0; ks < 4; ++ks) { const bf16x8 af = *(const LAS bf16x8*)(xr + 32 * ks); acc = __builtin_amdgcn_mfma_f32_32x32x16_bf16(af, src[q][ks], acc, 0, 0, 0); } } }
; __device__ __forceinline__ void compress_mfma_phase(Frame& F, int l, bf16* CMP) {
;     ...
;         { bf16x8 wa[4][4], wb[4][4]; const int l0 = 16 * lh;
;     ...
;           CMP_LOADW(wa, l0) CMP_LOADW(wb, l0 + 4) CMP_MMA(wa, l0) CMP_LOADW(wa, l0 + 8) CMP_MMA(wb, l0 + 4) CMP_LOADW(wb, l0 + 12) CMP_MMA(wa, l0 + 8) CMP_MMA(wb, l0 + 12)
	v_mfma_f32_32x32x16_bf16 v[2:17], v[212:215], v[174:177], v[2:17]
	global_load_dwordx4 v[174:177], v[220:221], off offset:1312
	ds_read_b128 v[212:215], v48 offset:38048
	s_waitcnt vmcnt(15) lgkmcnt(7)
	v_mfma_f32_32x32x16_bf16 v[2:17], v[216:219], v[178:181], v[2:17]
	global_load_dwordx4 v[178:181], v[220:221], off offset:1344
	ds_read_b128 v[216:219], v48 offset:38080
	s_waitcnt vmcnt(15) lgkmcnt(7)
	v_mfma_f32_32x32x16_bf16 v[2:17], v[80:83], v[182:185], v[2:17]
	global_load_dwordx4 v[182:185], v[220:221], off offset:1376
	ds_read_b128 v[80:83], v48 offset:38112
	s_waitcnt vmcnt(15) lgkmcnt(7)
	v_mfma_f32_32x32x16_bf16 v[2:17], v[84:87], v[186:189], v[2:17]
	global_load_dwordx4 v[186:189], v[220:221], off offset:1408
	ds_read_b128 v[84:87], v48 offset:42768
	s_waitcnt vmcnt(15) lgkmcnt(7)
	v_mfma_f32_32x32x16_bf16 v[2:17], v[88:91], v[190:193], v[2:17]
	global_load_dwordx4 v[190:193], v[220:221], off offset:1440
	ds_read_b128 v[88:91], v48 offset:42800
	s_waitcnt vmcnt(15) lgkmcnt(7)
	v_mfma_f32_32x32x16_bf16 v[2:17], v[92:95], v[200:203], v[2:17]
	global_load_dwordx4 v[200:203], v[220:221], off offset:1472
	ds_read_b128 v[92:95], v48 offset:42832
	s_waitcnt vmcnt(15) lgkmcnt(7)
	v_mfma_f32_32x32x16_bf16 v[2:17], v[96:99], v[204:207], v[2:17]
	global_load_dwordx4 v[204:207], v[220:221], off offset:1504
	ds_read_b128 v[96:99], v48 offset:42864
	s_waitcnt vmcnt(15) lgkmcnt(7)
	v_mfma_f32_32x32x16_bf16 v[2:17], v[208:211], v[138:141], v[2:17]
	global_load_dwordx4 v[138:141], v[220:221], off offset:1536
	ds_read_b128 v[208:211], v48 offset:47520
	s_waitcnt vmcnt(15) lgkmcnt(7)
	v_mfma_f32_32x32x16_bf16 v[2:17], v[212:215], v[142:145], v[2:17]
	global_load_dwordx4 v[142:145], v[220:221], off offset:1568
	ds_read_b128 v[212:215], v48 offset:47552
	s_waitcnt vmcnt(15) lgkmcnt(7)
	v_mfma_f32_32x32x16_bf16 v[2:17], v[216:219], v[146:149], v[2:17]
	global_load_dwordx4 v[146:149], v[220:221], off offset:1600
	ds_read_b128 v[216:219], v48 offset:47584
	s_waitcnt vmcnt(15) lgkmcnt(7)
	v_mfma_f32_32x32x16_bf16 v[2:17], v[80:83], v[150:153], v[2:17]
	global_load_dwordx4 v[150:153], v[220:221], off offset:1632
	ds_read_b128 v[80:83], v48 offset:47616
	s_waitcnt vmcnt(15) lgkmcnt(7)
	v_mfma_f32_32x32x16_bf16 v[2:17], v[84:87], v[154:157], v[2:17]
	global_load_dwordx4 v[154:157], v[220:221], off offset:1664
	ds_read_b128 v[84:87], v48 offset:52272
	s_waitcnt vmcnt(15) lgkmcnt(7)
	v_mfma_f32_32x32x16_bf16 v[2:17], v[88:91], v[158:161], v[2:17]
	global_load_dwordx4 v[158:161], v[220:221], off offset:1696
	ds_read_b128 v[88:91], v48 offset:52304
	s_waitcnt vmcnt(15) lgkmcnt(7)
	v_mfma_f32_32x32x16_bf16 v[2:17], v[92:95], v[162:165], v[2:17]
	global_load_dwordx4 v[162:165], v[220:221], off offset:1728
	ds_read_b128 v[92:95], v48 offset:52336
	s_waitcnt vmcnt(15) lgkmcnt(7)
	v_mfma_f32_32x32x16_bf16 v[2:17], v[96:99], v[166:169], v[2:17]
	global_load_dwordx4 v[166:169], v[220:221], off offset:1760
	ds_read_b128 v[96:99], v48 offset:52368
	s_waitcnt vmcnt(15) lgkmcnt(7)
	v_mfma_f32_32x32x16_bf16 v[2:17], v[208:211], v[170:173], v[2:17]
	global_load_dwordx4 v[170:173], v[220:221], off offset:1792
	ds_read_b128 v[208:211], v48 offset:57024
	s_waitcnt vmcnt(15) lgkmcnt(7)
	v_mfma_f32_32x32x16_bf16 v[2:17], v[212:215], v[174:177], v[2:17]
	global_load_dwordx4 v[174:177], v[220:221], off offset:1824
	ds_read_b128 v[212:215], v48 offset:57056
	s_waitcnt vmcnt(15) lgkmcnt(7)
	v_mfma_f32_32x32x16_bf16 v[2:17], v[216:219], v[178:181], v[2:17]
	global_load_dwordx4 v[178:181], v[220:221], off offset:1856
	ds_read_b128 v[216:219], v48 offset:57088
	s_waitcnt vmcnt(15) lgkmcnt(7)
	v_mfma_f32_32x32x16_bf16 v[2:17], v[80:83], v[182:185], v[2:17]
	global_load_dwordx4 v[182:185], v[220:221], off offset:1888
	ds_read_b128 v[80:83], v48 offset:57120
	s_waitcnt vmcnt(15) lgkmcnt(7)
	v_mfma_f32_32x32x16_bf16 v[2:17], v[84:87], v[186:189], v[2:17]
	global_load_dwordx4 v[186:189], v[220:221], off offset:1920
	ds_read_b128 v[84:87], v48 offset:61776
	s_waitcnt vmcnt(15) lgkmcnt(7)
	v_mfma_f32_32x32x16_bf16 v[2:17], v[88:91], v[190:193], v[2:17]
	global_load_dwordx4 v[190:193], v[220:221], off offset:1952
	ds_read_b128 v[88:91], v48 offset:61808
	s_waitcnt vmcnt(15) lgkmcnt(7)
	v_mfma_f32_32x32x16_bf16 v[2:17], v[92:95], v[200:203], v[2:17]
	global_load_dwordx4 v[200:203], v[220:221], off offset:1984
	ds_read_b128 v[92:95], v48 offset:61840
	s_waitcnt vmcnt(15) lgkmcnt(7)
	v_mfma_f32_32x32x16_bf16 v[2:17], v[96:99], v[204:207], v[2:17]
	global_load_dwordx4 v[204:207], v[220:221], off offset:2016
	ds_read_b128 v[96:99], v48 offset:61872
	s_waitcnt vmcnt(15) lgkmcnt(7)
	v_mfma_f32_32x32x16_bf16 v[2:17], v[208:211], v[138:141], v[2:17]
	ds_read_b128 v[208:211], v49
	s_waitcnt vmcnt(14) lgkmcnt(7)
	v_mfma_f32_32x32x16_bf16 v[2:17], v[212:215], v[142:145], v[2:17]
	ds_read_b128 v[212:215], v50
	s_waitcnt vmcnt(13) lgkmcnt(7)
	v_mfma_f32_32x32x16_bf16 v[2:17], v[216:219], v[146:149], v[2:17]
	ds_read_b128 v[216:219], v51
	s_waitcnt vmcnt(12) lgkmcnt(7)
	v_mfma_f32_32x32x16_bf16 v[2:17], v[80:83], v[150:153], v[2:17]
	ds_read_b128 v[80:83], v52
	s_waitcnt vmcnt(11) lgkmcnt(7)
	v_mfma_f32_32x32x16_bf16 v[2:17], v[84:87], v[154:157], v[2:17]
	ds_read_b128 v[84:87], v53
	s_waitcnt vmcnt(10) lgkmcnt(7)
	v_mfma_f32_32x32x16_bf16 v[2:17], v[88:91], v[158:161], v[2:17]
	ds_read_b128 v[88:91], v54
	s_waitcnt vmcnt(9) lgkmcnt(7)
	v_mfma_f32_32x32x16_bf16 v[2:17], v[92:95], v[162:165], v[2:17]
	ds_read_b128 v[92:95], v55
	s_waitcnt vmcnt(8) lgkmcnt(7)
	v_mfma_f32_32x32x16_bf16 v[2:17], v[96:99], v[166:169], v[2:17]
	ds_read_b128 v[96:99], v56
	s_waitcnt vmcnt(7) lgkmcnt(7)
	v_mfma_f32_32x32x16_bf16 v[2:17], v[208:211], v[170:173], v[2:17]
	s_waitcnt vmcnt(6) lgkmcnt(6)
	v_mfma_f32_32x32x16_bf16 v[2:17], v[212:215], v[174:177], v[2:17]
	s_waitcnt vmcnt(5) lgkmcnt(5)
	v_mfma_f32_32x32x16_bf16 v[2:17], v[216:219], v[178:181], v[2:17]
	s_waitcnt vmcnt(4) lgkmcnt(4)
	v_mfma_f32_32x32x16_bf16 v[2:17], v[80:83], v[182:185], v[2:17]
	s_waitcnt vmcnt(3) lgkmcnt(3)
	v_mfma_f32_32x32x16_bf16 v[2:17], v[84:87], v[186:189], v[2:17]
	s_waitcnt vmcnt(2) lgkmcnt(2)
	v_mfma_f32_32x32x16_bf16 v[2:17], v[88:91], v[190:193], v[2:17]
	s_waitcnt vmcnt(1) lgkmcnt(1)
	v_mfma_f32_32x32x16_bf16 v[2:17], v[92:95], v[200:203], v[2:17]
	s_waitcnt vmcnt(0) lgkmcnt(0)
	v_mfma_f32_32x32x16_bf16 v[2:17], v[96:99], v[204:207], v[2:17]
	v_readlane_b32 s2, v246, 15
	v_readlane_b32 s3, v246, 16
	s_andn2_b64 vcc, exec, s[2:3]
	s_cbranch_vccnz .LBB0_381
; __device__ __forceinline__ void compress_mfma_phase(Frame& F, int l, bf16* CMP) {
;     ...
;         if (lh == 1) {
; #pragma unroll
;             for (int r = 0; r < 16; ++r) RED[((r & 3) + 8 * (r >> 2) + 4 * h) * 129 + 32 * ct + r32] = acc[r]; }
	v_add_u32_e32 v0, 0x400, v78
	s_nop 9
	ds_write2_b32 v0, v4, v5 offset0:2 offset1:131
	v_add_u32_e32 v0, 0x1000, v78
	ds_write2_b32 v0, v6, v7 offset0:8 offset1:137
	v_add_u32_e32 v0, 0x1400, v78
	ds_write2_b32 v0, v8, v9 offset0:10 offset1:139
	v_add_u32_e32 v0, 0x2000, v78
	ds_write2_b32 v0, v10, v11 offset0:16 offset1:145
	v_add_u32_e32 v0, 0x2400, v78
	ds_write2_b32 v0, v12, v13 offset0:18 offset1:147
	v_add_u32_e32 v0, 0x3000, v78
	ds_write2_b32 v0, v14, v15 offset0:24 offset1:153
	v_add_u32_e32 v0, 0x3400, v78
	ds_write2_b32 v78, v2, v3 offset1:129
	ds_write2_b32 v0, v16, v17 offset0:26 offset1:155
